# grid barrier: L1 invalidate issued right after the arrival atomic (overlaps the wait) + P5 epilogue scale loads hoisted; on top of P1/P3 epilogue rewrites
# speedup vs baseline: 1.0095x; 1.0055x over previous
; __device__ __forceinline__ unsigned xb_ld(unsigned* p)              { return __hip_atomic_load(p, __ATOMIC_RELAXED, __HIP_MEMORY_SCOPE_AGENT); }
; __device__ __forceinline__ unsigned xb_add(unsigned* p, unsigned v) { return __hip_atomic_fetch_add(p, v, __ATOMIC_RELAXED, __HIP_MEMORY_SCOPE_AGENT); }
; #define XB_SPIN(cond, bar) do { unsigned _sp = 0; while (cond) { __builtin_amdgcn_s_sleep(1); \
;     if ((++_sp & 255u) == 0u) { if (xb_ld(&(bar)[XB_TMO])) break; if (_sp > XB_SPIN_CAP) { atomicAdd(&(bar)[XB_TMO], 1u); break; } } } } while (0)
; __device__ __forceinline__ void xcd_barrier(const XcdBarrier& b) {
;     ...
;         const unsigned old = xb_add(&bar[XB_XSUB(b.x)], 1u);
;         const unsigned gen = old / nloc;
;         if (old + 1u == (gen + 1u) * nloc) {
;             __builtin_amdgcn_fence(__ATOMIC_RELEASE, "agent");
;             asm volatile("s_waitcnt vmcnt(0)" ::: "memory");
;             const unsigned og = xb_add(&bar[XB_TOP], 1u);
;             const unsigned tg = og / nx;
;             if (og + 1u == (tg + 1u) * nx) xb_add(&bar[XB_TOPGEN], 1u);
;             else XB_SPIN(xb_ld(&bar[XB_TOPGEN]) == tg, bar);
;             __builtin_amdgcn_fence(__ATOMIC_ACQUIRE, "agent");
;             xb_add(&bar[XB_XGEN(b.x)], 1u);
;             asm volatile("s_waitcnt vmcnt(0)" ::: "memory");
;         } else {
;             XB_SPIN(xb_ld(&bar[XB_XGEN(b.x)]) == gen, bar);
.LBB0_99:
	s_or_b64 exec, exec, s[6:7]
	buffer_inv sc1
	v_cvt_f32_u32_e32 v5, v3
	s_waitcnt vmcnt(1)
	v_readfirstlane_b32 s6, v4
	v_sub_u32_e32 v4, 0, v3
	v_rcp_iflag_f32_e32 v5, v5
	v_add_u32_e32 v6, s6, v2
	v_mul_f32_e32 v5, 0x4f7ffffe, v5
	v_cvt_u32_f32_e32 v5, v5
	v_mul_lo_u32 v2, v4, v5
	v_mul_hi_u32 v2, v5, v2
	v_add_u32_e32 v2, v5, v2
	v_mul_hi_u32 v2, v6, v2
	v_mul_lo_u32 v4, v2, v3
	v_sub_u32_e32 v4, v6, v4
	v_add_u32_e32 v5, 1, v2
	v_sub_u32_e32 v7, v4, v3
	v_cmp_ge_u32_e32 vcc, v4, v3
	s_nop 1
	v_cndmask_b32_e32 v2, v2, v5, vcc
	v_cndmask_b32_e32 v4, v4, v7, vcc
	v_add_u32_e32 v5, 1, v2
	v_cmp_ge_u32_e32 vcc, v4, v3
	v_add_u32_e32 v4, 1, v6
	s_nop 0
	v_cndmask_b32_e32 v2, v2, v5, vcc
	v_mul_lo_u32 v5, v3, v2
	v_add_u32_e32 v3, v5, v3
	v_cmp_ne_u32_e32 vcc, v4, v3
	s_and_saveexec_b64 s[6:7], vcc
	s_xor_b64 s[6:7], exec, s[6:7]
	s_cbranch_execz .LBB0_113
	s_waitcnt lgkmcnt(0)
	v_mov_b32_e32 v1, 0
	global_load_dword v3, v1, s[16:17] sc1
	s_waitcnt vmcnt(0)
	v_cmp_eq_u32_e32 vcc, v3, v2
	s_and_saveexec_b64 s[36:37], vcc
	s_cbranch_execz .LBB0_112
	s_mov_b32 s8, 1
	s_mov_b64 s[38:39], 0
	s_branch .LBB0_103

; __device__ __forceinline__ unsigned xb_ld(unsigned* p)              { return __hip_atomic_load(p, __ATOMIC_RELAXED, __HIP_MEMORY_SCOPE_AGENT); }
; #define XB_SPIN(cond, bar) do { unsigned _sp = 0; while (cond) { __builtin_amdgcn_s_sleep(1); \
;     if ((++_sp & 255u) == 0u) { if (xb_ld(&(bar)[XB_TMO])) break; if (_sp > XB_SPIN_CAP) { atomicAdd(&(bar)[XB_TMO], 1u); break; } } } } while (0)
; __device__ __forceinline__ void xcd_barrier(const XcdBarrier& b) {
;     ...
;             XB_SPIN(xb_ld(&bar[XB_XGEN(b.x)]) == gen, bar);
;             __builtin_amdgcn_fence(__ATOMIC_ACQUIRE, "agent");
;             asm volatile("s_waitcnt vmcnt(0)" ::: "memory");
.LBB0_112:
	s_or_b64 exec, exec, s[36:37]
	s_waitcnt vmcnt(0)
	s_waitcnt vmcnt(0)

; __device__ __forceinline__ unsigned xb_ld(unsigned* p)              { return __hip_atomic_load(p, __ATOMIC_RELAXED, __HIP_MEMORY_SCOPE_AGENT); }
; __device__ __forceinline__ unsigned xb_add(unsigned* p, unsigned v) { return __hip_atomic_fetch_add(p, v, __ATOMIC_RELAXED, __HIP_MEMORY_SCOPE_AGENT); }
; #define XB_SPIN(cond, bar) do { unsigned _sp = 0; while (cond) { __builtin_amdgcn_s_sleep(1); \
;     if ((++_sp & 255u) == 0u) { if (xb_ld(&(bar)[XB_TMO])) break; if (_sp > XB_SPIN_CAP) { atomicAdd(&(bar)[XB_TMO], 1u); break; } } } } while (0)
; __device__ __forceinline__ void xcd_barrier(const XcdBarrier& b) {
;     ...
;             else XB_SPIN(xb_ld(&bar[XB_TOPGEN]) == tg, bar);
;             __builtin_amdgcn_fence(__ATOMIC_ACQUIRE, "agent");
;             xb_add(&bar[XB_XGEN(b.x)], 1u);
;             asm volatile("s_waitcnt vmcnt(0)" ::: "memory");
.LBB0_130:
	s_or_b64 exec, exec, s[6:7]
	s_mov_b64 s[6:7], exec
	v_mbcnt_lo_u32_b32 v1, s6, 0
	v_mbcnt_hi_u32_b32 v1, s7, v1
	v_cmp_eq_u32_e32 vcc, 0, v1
	s_waitcnt vmcnt(0)
	s_and_saveexec_b64 s[36:37], vcc
	s_cbranch_execz .LBB0_132
	s_bcnt1_i32_b64 s6, s[6:7]
	v_mov_b32_e32 v1, 0
	v_mov_b32_e32 v2, s6
	global_atomic_add v1, v2, s[16:17]

; __device__ __forceinline__ unsigned xb_ld(unsigned* p)              { return __hip_atomic_load(p, __ATOMIC_RELAXED, __HIP_MEMORY_SCOPE_AGENT); }
; __device__ __forceinline__ unsigned xb_add(unsigned* p, unsigned v) { return __hip_atomic_fetch_add(p, v, __ATOMIC_RELAXED, __HIP_MEMORY_SCOPE_AGENT); }
; #define XB_SPIN(cond, bar) do { unsigned _sp = 0; while (cond) { __builtin_amdgcn_s_sleep(1); \
;     if ((++_sp & 255u) == 0u) { if (xb_ld(&(bar)[XB_TMO])) break; if (_sp > XB_SPIN_CAP) { atomicAdd(&(bar)[XB_TMO], 1u); break; } } } } while (0)
; __device__ __forceinline__ void xcd_barrier(const XcdBarrier& b) {
;     ...
;         const unsigned old = xb_add(&bar[XB_XSUB(b.x)], 1u);
;         const unsigned gen = old / nloc;
;         if (old + 1u == (gen + 1u) * nloc) {
;             __builtin_amdgcn_fence(__ATOMIC_RELEASE, "agent");
;             asm volatile("s_waitcnt vmcnt(0)" ::: "memory");
;             const unsigned og = xb_add(&bar[XB_TOP], 1u);
;             const unsigned tg = og / nx;
;             if (og + 1u == (tg + 1u) * nx) xb_add(&bar[XB_TOPGEN], 1u);
;             else XB_SPIN(xb_ld(&bar[XB_TOPGEN]) == tg, bar);
;             __builtin_amdgcn_fence(__ATOMIC_ACQUIRE, "agent");
;             xb_add(&bar[XB_XGEN(b.x)], 1u);
;             asm volatile("s_waitcnt vmcnt(0)" ::: "memory");
;         } else {
;             XB_SPIN(xb_ld(&bar[XB_XGEN(b.x)]) == gen, bar);
.LBB0_172:
	s_or_b64 exec, exec, s[4:5]
	buffer_inv sc1
	v_cvt_f32_u32_e32 v6, v4
	s_waitcnt vmcnt(1)
	v_readfirstlane_b32 s4, v5
	v_sub_u32_e32 v5, 0, v4
	v_rcp_iflag_f32_e32 v6, v6
	v_add_u32_e32 v7, s4, v3
	v_mul_f32_e32 v6, 0x4f7ffffe, v6
	v_cvt_u32_f32_e32 v6, v6
	v_mul_lo_u32 v3, v5, v6
	v_mul_hi_u32 v3, v6, v3
	v_add_u32_e32 v3, v6, v3
	v_mul_hi_u32 v3, v7, v3
	v_mul_lo_u32 v5, v3, v4
	v_sub_u32_e32 v5, v7, v5
	v_add_u32_e32 v6, 1, v3
	v_cmp_ge_u32_e32 vcc, v5, v4
	s_nop 1
	v_cndmask_b32_e32 v3, v3, v6, vcc
	v_sub_u32_e32 v6, v5, v4
	v_cndmask_b32_e32 v5, v5, v6, vcc
	v_add_u32_e32 v6, 1, v3
	v_cmp_ge_u32_e32 vcc, v5, v4
	v_add_u32_e32 v5, 1, v7
	s_nop 0
	v_cndmask_b32_e32 v3, v3, v6, vcc
	v_mul_lo_u32 v6, v4, v3
	v_add_u32_e32 v4, v6, v4
	v_cmp_ne_u32_e32 vcc, v5, v4
	s_and_saveexec_b64 s[4:5], vcc
	s_xor_b64 s[4:5], exec, s[4:5]
	s_cbranch_execz .LBB0_186
	s_waitcnt lgkmcnt(0)
	v_mov_b32_e32 v2, 0
	global_load_dword v4, v2, s[16:17] sc1
	s_waitcnt vmcnt(0)
	v_cmp_eq_u32_e32 vcc, v4, v3
	s_and_saveexec_b64 s[6:7], vcc
	s_cbranch_execz .LBB0_185
	s_mov_b32 s8, 1
	s_mov_b64 s[38:39], 0
	s_branch .LBB0_176

; __device__ __forceinline__ unsigned xb_ld(unsigned* p)              { return __hip_atomic_load(p, __ATOMIC_RELAXED, __HIP_MEMORY_SCOPE_AGENT); }
; #define XB_SPIN(cond, bar) do { unsigned _sp = 0; while (cond) { __builtin_amdgcn_s_sleep(1); \
;     if ((++_sp & 255u) == 0u) { if (xb_ld(&(bar)[XB_TMO])) break; if (_sp > XB_SPIN_CAP) { atomicAdd(&(bar)[XB_TMO], 1u); break; } } } } while (0)
; __device__ __forceinline__ void xcd_barrier(const XcdBarrier& b) {
;     ...
;             XB_SPIN(xb_ld(&bar[XB_XGEN(b.x)]) == gen, bar);
;             __builtin_amdgcn_fence(__ATOMIC_ACQUIRE, "agent");
;             asm volatile("s_waitcnt vmcnt(0)" ::: "memory");
.LBB0_185:
	s_or_b64 exec, exec, s[6:7]
	s_waitcnt vmcnt(0)
	s_waitcnt vmcnt(0)

; __device__ __forceinline__ unsigned xb_ld(unsigned* p)              { return __hip_atomic_load(p, __ATOMIC_RELAXED, __HIP_MEMORY_SCOPE_AGENT); }
; __device__ __forceinline__ unsigned xb_add(unsigned* p, unsigned v) { return __hip_atomic_fetch_add(p, v, __ATOMIC_RELAXED, __HIP_MEMORY_SCOPE_AGENT); }
; #define XB_SPIN(cond, bar) do { unsigned _sp = 0; while (cond) { __builtin_amdgcn_s_sleep(1); \
;     if ((++_sp & 255u) == 0u) { if (xb_ld(&(bar)[XB_TMO])) break; if (_sp > XB_SPIN_CAP) { atomicAdd(&(bar)[XB_TMO], 1u); break; } } } } while (0)
; __device__ __forceinline__ void xcd_barrier(const XcdBarrier& b) {
;     ...
;             else XB_SPIN(xb_ld(&bar[XB_TOPGEN]) == tg, bar);
;             __builtin_amdgcn_fence(__ATOMIC_ACQUIRE, "agent");
;             xb_add(&bar[XB_XGEN(b.x)], 1u);
;             asm volatile("s_waitcnt vmcnt(0)" ::: "memory");
.LBB0_203:
	s_or_b64 exec, exec, s[4:5]
	s_mov_b64 s[4:5], exec
	v_mbcnt_lo_u32_b32 v2, s4, 0
	v_mbcnt_hi_u32_b32 v2, s5, v2
	v_cmp_eq_u32_e32 vcc, 0, v2
	s_waitcnt vmcnt(0)
	s_and_saveexec_b64 s[6:7], vcc
	s_cbranch_execz .LBB0_205
	s_bcnt1_i32_b64 s4, s[4:5]
	v_mov_b32_e32 v2, 0
	v_mov_b32_e32 v3, s4
	global_atomic_add v2, v3, s[16:17]

; __device__ __forceinline__ unsigned xb_ld(unsigned* p)              { return __hip_atomic_load(p, __ATOMIC_RELAXED, __HIP_MEMORY_SCOPE_AGENT); }
; __device__ __forceinline__ unsigned xb_add(unsigned* p, unsigned v) { return __hip_atomic_fetch_add(p, v, __ATOMIC_RELAXED, __HIP_MEMORY_SCOPE_AGENT); }
; #define XB_SPIN(cond, bar) do { unsigned _sp = 0; while (cond) { __builtin_amdgcn_s_sleep(1); \
;     if ((++_sp & 255u) == 0u) { if (xb_ld(&(bar)[XB_TMO])) break; if (_sp > XB_SPIN_CAP) { atomicAdd(&(bar)[XB_TMO], 1u); break; } } } } while (0)
; __device__ __forceinline__ void xcd_barrier(const XcdBarrier& b) {
;     ...
;         const unsigned old = xb_add(&bar[XB_XSUB(b.x)], 1u);
;         const unsigned gen = old / nloc;
;         if (old + 1u == (gen + 1u) * nloc) {
;             __builtin_amdgcn_fence(__ATOMIC_RELEASE, "agent");
;             asm volatile("s_waitcnt vmcnt(0)" ::: "memory");
;             const unsigned og = xb_add(&bar[XB_TOP], 1u);
;             const unsigned tg = og / nx;
;             if (og + 1u == (tg + 1u) * nx) xb_add(&bar[XB_TOPGEN], 1u);
;             else XB_SPIN(xb_ld(&bar[XB_TOPGEN]) == tg, bar);
;             __builtin_amdgcn_fence(__ATOMIC_ACQUIRE, "agent");
;             xb_add(&bar[XB_XGEN(b.x)], 1u);
;             asm volatile("s_waitcnt vmcnt(0)" ::: "memory");
;         } else {
;             XB_SPIN(xb_ld(&bar[XB_XGEN(b.x)]) == gen, bar);
.LBB0_368:
	s_or_b64 exec, exec, s[4:5]
	buffer_inv sc1
	v_cvt_f32_u32_e32 v6, v4
	s_waitcnt vmcnt(1)
	v_readfirstlane_b32 s4, v5
	v_sub_u32_e32 v5, 0, v4
	v_rcp_iflag_f32_e32 v6, v6
	v_add_u32_e32 v7, s4, v3
	v_mul_f32_e32 v6, 0x4f7ffffe, v6
	v_cvt_u32_f32_e32 v6, v6
	v_mul_lo_u32 v3, v5, v6
	v_mul_hi_u32 v3, v6, v3
	v_add_u32_e32 v3, v6, v3
	v_mul_hi_u32 v3, v7, v3
	v_mul_lo_u32 v5, v3, v4
	v_sub_u32_e32 v5, v7, v5
	v_add_u32_e32 v6, 1, v3
	v_cmp_ge_u32_e32 vcc, v5, v4
	s_nop 1
	v_cndmask_b32_e32 v3, v3, v6, vcc
	v_sub_u32_e32 v6, v5, v4
	v_cndmask_b32_e32 v5, v5, v6, vcc
	v_add_u32_e32 v6, 1, v3
	v_cmp_ge_u32_e32 vcc, v5, v4
	v_add_u32_e32 v5, 1, v7
	s_nop 0
	v_cndmask_b32_e32 v3, v3, v6, vcc
	v_mul_lo_u32 v6, v4, v3
	v_add_u32_e32 v4, v6, v4
	v_cmp_ne_u32_e32 vcc, v5, v4
	s_and_saveexec_b64 s[4:5], vcc
	s_xor_b64 s[4:5], exec, s[4:5]
	s_cbranch_execz .LBB0_382
	s_waitcnt lgkmcnt(0)
	v_mov_b32_e32 v2, 0
	global_load_dword v4, v2, s[16:17] sc1
	s_waitcnt vmcnt(0)
	v_cmp_eq_u32_e32 vcc, v4, v3
	s_and_saveexec_b64 s[6:7], vcc
	s_cbranch_execz .LBB0_381
	s_mov_b32 s8, 1
	s_mov_b64 s[40:41], 0
	s_branch .LBB0_372

; __device__ __forceinline__ unsigned xb_ld(unsigned* p)              { return __hip_atomic_load(p, __ATOMIC_RELAXED, __HIP_MEMORY_SCOPE_AGENT); }
; __device__ __forceinline__ unsigned xb_add(unsigned* p, unsigned v) { return __hip_atomic_fetch_add(p, v, __ATOMIC_RELAXED, __HIP_MEMORY_SCOPE_AGENT); }
; #define XB_SPIN(cond, bar) do { unsigned _sp = 0; while (cond) { __builtin_amdgcn_s_sleep(1); \
;     if ((++_sp & 255u) == 0u) { if (xb_ld(&(bar)[XB_TMO])) break; if (_sp > XB_SPIN_CAP) { atomicAdd(&(bar)[XB_TMO], 1u); break; } } } } while (0)
; __device__ __forceinline__ void xcd_barrier(const XcdBarrier& b) {
;     ...
;         const unsigned old = xb_add(&bar[XB_XSUB(b.x)], 1u);
;         const unsigned gen = old / nloc;
;         if (old + 1u == (gen + 1u) * nloc) {
;             __builtin_amdgcn_fence(__ATOMIC_RELEASE, "agent");
;             asm volatile("s_waitcnt vmcnt(0)" ::: "memory");
;             const unsigned og = xb_add(&bar[XB_TOP], 1u);
;             const unsigned tg = og / nx;
;             if (og + 1u == (tg + 1u) * nx) xb_add(&bar[XB_TOPGEN], 1u);
;             else XB_SPIN(xb_ld(&bar[XB_TOPGEN]) == tg, bar);
;             __builtin_amdgcn_fence(__ATOMIC_ACQUIRE, "agent");
;             xb_add(&bar[XB_XGEN(b.x)], 1u);
;             asm volatile("s_waitcnt vmcnt(0)" ::: "memory");
;         } else {
;             XB_SPIN(xb_ld(&bar[XB_XGEN(b.x)]) == gen, bar);
.LBB0_505:
	s_or_b64 exec, exec, s[6:7]
	buffer_inv sc1
	v_cvt_f32_u32_e32 v6, v4
	s_waitcnt vmcnt(1)
	v_readfirstlane_b32 s6, v5
	v_sub_u32_e32 v5, 0, v4
	v_rcp_iflag_f32_e32 v6, v6
	v_add_u32_e32 v7, s6, v3
	v_mul_f32_e32 v6, 0x4f7ffffe, v6
	v_cvt_u32_f32_e32 v6, v6
	v_mul_lo_u32 v3, v5, v6
	v_mul_hi_u32 v3, v6, v3
	v_add_u32_e32 v3, v6, v3
	v_mul_hi_u32 v3, v7, v3
	v_mul_lo_u32 v5, v3, v4
	v_sub_u32_e32 v5, v7, v5
	v_add_u32_e32 v6, 1, v3
	v_cmp_ge_u32_e32 vcc, v5, v4
	s_nop 1
	v_cndmask_b32_e32 v3, v3, v6, vcc
	v_sub_u32_e32 v6, v5, v4
	v_cndmask_b32_e32 v5, v5, v6, vcc
	v_add_u32_e32 v6, 1, v3
	v_cmp_ge_u32_e32 vcc, v5, v4
	v_add_u32_e32 v5, 1, v7
	s_nop 0
	v_cndmask_b32_e32 v3, v3, v6, vcc
	v_mul_lo_u32 v6, v4, v3
	v_add_u32_e32 v4, v6, v4
	v_cmp_ne_u32_e32 vcc, v5, v4
	s_and_saveexec_b64 s[6:7], vcc
	s_xor_b64 s[6:7], exec, s[6:7]
	s_cbranch_execz .LBB0_519
	s_waitcnt lgkmcnt(0)
	v_mov_b32_e32 v2, 0
	global_load_dword v4, v2, s[16:17] sc1
	s_waitcnt vmcnt(0)
	v_cmp_eq_u32_e32 vcc, v4, v3
	s_and_saveexec_b64 s[38:39], vcc
	s_cbranch_execz .LBB0_518
	s_mov_b32 s8, 1
	s_mov_b64 s[40:41], 0
	s_branch .LBB0_509

; __device__ __forceinline__ unsigned xb_ld(unsigned* p)              { return __hip_atomic_load(p, __ATOMIC_RELAXED, __HIP_MEMORY_SCOPE_AGENT); }
; #define XB_SPIN(cond, bar) do { unsigned _sp = 0; while (cond) { __builtin_amdgcn_s_sleep(1); \
;     if ((++_sp & 255u) == 0u) { if (xb_ld(&(bar)[XB_TMO])) break; if (_sp > XB_SPIN_CAP) { atomicAdd(&(bar)[XB_TMO], 1u); break; } } } } while (0)
; __device__ __forceinline__ void xcd_barrier(const XcdBarrier& b) {
;     ...
;             XB_SPIN(xb_ld(&bar[XB_XGEN(b.x)]) == gen, bar);
;             __builtin_amdgcn_fence(__ATOMIC_ACQUIRE, "agent");
;             asm volatile("s_waitcnt vmcnt(0)" ::: "memory");
.LBB0_518:
	s_or_b64 exec, exec, s[38:39]
	s_waitcnt vmcnt(0)
	s_waitcnt vmcnt(0)

; __device__ __forceinline__ unsigned xb_ld(unsigned* p)              { return __hip_atomic_load(p, __ATOMIC_RELAXED, __HIP_MEMORY_SCOPE_AGENT); }
; __device__ __forceinline__ unsigned xb_add(unsigned* p, unsigned v) { return __hip_atomic_fetch_add(p, v, __ATOMIC_RELAXED, __HIP_MEMORY_SCOPE_AGENT); }
; #define XB_SPIN(cond, bar) do { unsigned _sp = 0; while (cond) { __builtin_amdgcn_s_sleep(1); \
;     if ((++_sp & 255u) == 0u) { if (xb_ld(&(bar)[XB_TMO])) break; if (_sp > XB_SPIN_CAP) { atomicAdd(&(bar)[XB_TMO], 1u); break; } } } } while (0)
; __device__ __forceinline__ void xcd_barrier(const XcdBarrier& b) {
;     ...
;             else XB_SPIN(xb_ld(&bar[XB_TOPGEN]) == tg, bar);
;             __builtin_amdgcn_fence(__ATOMIC_ACQUIRE, "agent");
;             xb_add(&bar[XB_XGEN(b.x)], 1u);
;             asm volatile("s_waitcnt vmcnt(0)" ::: "memory");
.LBB0_536:
	s_or_b64 exec, exec, s[6:7]
	s_mov_b64 s[6:7], exec
	v_mbcnt_lo_u32_b32 v2, s6, 0
	v_mbcnt_hi_u32_b32 v2, s7, v2
	v_cmp_eq_u32_e32 vcc, 0, v2
	s_waitcnt vmcnt(0)
	s_and_saveexec_b64 s[38:39], vcc
	s_cbranch_execz .LBB0_538
	s_bcnt1_i32_b64 s6, s[6:7]
	v_mov_b32_e32 v2, 0
	v_mov_b32_e32 v3, s6
	global_atomic_add v2, v3, s[16:17]

; __device__ __forceinline__ unsigned cvt_pk_bf16(float lo, float hi) { unsigned r; asm volatile("v_cvt_pk_bf16_f32 %0, %1, %2" : "=v"(r) : "v"(lo), "v"(hi)); return r; }
;     __device__ __forceinline__ void operator()(const f32x4 (&acc)[2][2][4][2], const Unit& u, int wr, int wc, int fr, int fq) const {
;         const int row0 = u.pm * BM + wr * 64 + fr, col0 = u.pn * BM + wc * 32 + 8 * fq;
; #pragma unroll
;         for (int bj = 0; bj < 2; ++bj) {
;             const f32x4 s0 = *(const f32x4*)(sb + col0 + bj * HALF), s1 = *(const f32x4*)(sb + col0 + bj * HALF + 4);
; #pragma unroll
;             for (int ai = 0; ai < 2; ++ai)
; #pragma unroll
;                 for (int m = 0; m < 4; ++m) { const int row = row0 + ai * HALF + m * 16; bf16_t* rowp = O + (size_t)row * ldc + col0 + bj * HALF;
;                     f32x4 v0, v1;
;                     if constexpr (I8) { const float ra = sa[row]; const i32x4 i0 = __builtin_bit_cast(i32x4, acc[ai][bj][m][0]), i1 = __builtin_bit_cast(i32x4, acc[ai][bj][m][1]);
;                         v0 = __builtin_convertvector(i0, f32x4) * ra * s0; v1 = __builtin_convertvector(i1, f32x4) * ra * s1; }
;                     else { v0 = acc[ai][bj][m][0] * s0; v1 = acc[ai][bj][m][1] * s1; }
;                     u32x4 w; w.x = cvt_pk_bf16(v0[0], v0[1]); w.y = cvt_pk_bf16(v0[2], v0[3]); w.z = cvt_pk_bf16(v1[0], v1[1]); w.w = cvt_pk_bf16(v1[2], v1[3]);
;                     *(u32x4*)rowp = w; }
.LBB0_629:
	v_lshl_add_u32 v156, s54, 8, v160
	v_lshl_or_b32 v150, s63, 8, v161
	v_readlane_b32 s6, v243, 4
	v_ashrrev_i32_e32 v151, 31, v150
	v_readlane_b32 s7, v243, 5
	v_ashrrev_i32_e32 v157, 31, v156
	v_lshlrev_b64 v[158:159], 1, v[150:151]
	v_lshl_add_u64 v[154:155], v[150:151], 2, s[6:7]
	v_lshl_add_u64 v[150:151], v[156:157], 2, s[40:41]
	global_load_dwordx4 v[106:109], v[154:155], off offset:16
	global_load_dwordx4 v[114:117], v[154:155], off
	global_load_dword v164, v[150:151], off
	global_load_dword v180, v[150:151], off offset:64
	global_load_dword v182, v[150:151], off offset:128
	global_load_dword v184, v[150:151], off offset:192
	global_load_dword v186, v[150:151], off offset:512
	global_load_dword v188, v[150:151], off offset:576
	global_load_dword v190, v[150:151], off offset:640
	global_load_dword v192, v[150:151], off offset:704
	global_load_dword v178, v[150:151], off
	global_load_dwordx4 v[194:197], v[154:155], off offset:528
	global_load_dwordx4 v[198:201], v[154:155], off offset:512
	v_cvt_f32_i32_e32 v133, v133
	v_cvt_f32_i32_e32 v132, v132
	v_cvt_f32_i32_e32 v131, v131
	v_cvt_f32_i32_e32 v130, v130
	v_cvt_f32_i32_e32 v137, v137
	v_cvt_f32_i32_e32 v136, v136
	v_cvt_f32_i32_e32 v135, v135
	v_cvt_f32_i32_e32 v134, v134
	v_lshlrev_b64 v[152:153], 12, v[156:157]
	v_lshl_add_u64 v[152:153], s[74:75], 0, v[152:153]
	v_lshl_add_u64 v[152:153], v[152:153], 0, v[158:159]
	v_cvt_f32_i32_e32 v125, v125
	v_cvt_f32_i32_e32 v124, v124
	v_cvt_f32_i32_e32 v123, v123
	v_cvt_f32_i32_e32 v122, v122
	v_cvt_f32_i32_e32 v129, v129
	v_cvt_f32_i32_e32 v128, v128
	v_cvt_f32_i32_e32 v127, v127
	v_cvt_f32_i32_e32 v126, v126
	v_cvt_f32_i32_e32 v113, v113
	v_cvt_f32_i32_e32 v112, v112
	v_cvt_f32_i32_e32 v111, v111
	v_cvt_f32_i32_e32 v110, v110
	v_cvt_f32_i32_e32 v121, v121
	v_cvt_f32_i32_e32 v120, v120
	v_cvt_f32_i32_e32 v119, v119
	v_cvt_f32_i32_e32 v118, v118
	v_cvt_f32_i32_e32 v101, v101
	v_cvt_f32_i32_e32 v100, v100
	v_cvt_f32_i32_e32 v99, v99
	v_cvt_f32_i32_e32 v98, v98
	v_cvt_f32_i32_e32 v105, v105
	v_cvt_f32_i32_e32 v104, v104
	v_cvt_f32_i32_e32 v103, v103
	v_cvt_f32_i32_e32 v102, v102
	v_cvt_f32_i32_e32 v95, v95
	v_cvt_f32_i32_e32 v94, v94
	v_cvt_f32_i32_e32 v93, v93
	v_cvt_f32_i32_e32 v92, v92
	v_cvt_f32_i32_e32 v91, v91
	v_cvt_f32_i32_e32 v90, v90
	v_cvt_f32_i32_e32 v97, v97
	v_cvt_f32_i32_e32 v96, v96
	s_mov_b64 s[6:7], 0x80000
	v_cvt_f32_i32_e32 v87, v87
	v_cvt_f32_i32_e32 v86, v86
	v_cvt_f32_i32_e32 v85, v85
	v_cvt_f32_i32_e32 v84, v84
	v_cvt_f32_i32_e32 v83, v83
	v_cvt_f32_i32_e32 v82, v82
	v_cvt_f32_i32_e32 v89, v89
	v_cvt_f32_i32_e32 v88, v88
	v_cvt_f32_i32_e32 v79, v79
	v_cvt_f32_i32_e32 v78, v78
	v_cvt_f32_i32_e32 v77, v77
	v_cvt_f32_i32_e32 v76, v76
	v_cvt_f32_i32_e32 v75, v75
	v_cvt_f32_i32_e32 v74, v74
	v_cvt_f32_i32_e32 v81, v81
	v_cvt_f32_i32_e32 v80, v80
	v_cvt_f32_i32_e32 v71, v71
	v_cvt_f32_i32_e32 v70, v70
	v_cvt_f32_i32_e32 v69, v69
	v_cvt_f32_i32_e32 v68, v68
	v_cvt_f32_i32_e32 v67, v67
	v_cvt_f32_i32_e32 v66, v66
	v_cvt_f32_i32_e32 v73, v73
	v_cvt_f32_i32_e32 v72, v72
	v_cvt_f32_i32_e32 v61, v61
	v_cvt_f32_i32_e32 v60, v60
	v_cvt_f32_i32_e32 v59, v59
	v_cvt_f32_i32_e32 v58, v58
	v_cvt_f32_i32_e32 v65, v65
	v_cvt_f32_i32_e32 v64, v64
	v_cvt_f32_i32_e32 v63, v63
	v_cvt_f32_i32_e32 v62, v62
	v_cvt_f32_i32_e32 v53, v53
	v_cvt_f32_i32_e32 v52, v52
	v_cvt_f32_i32_e32 v51, v51
	s_waitcnt vmcnt(0)
	v_pk_mul_f32 v[130:131], v[164:165], v[130:131] op_sel_hi:[0,1]
	v_pk_mul_f32 v[132:133], v[164:165], v[132:133] op_sel_hi:[0,1]
	v_pk_mul_f32 v[134:135], v[164:165], v[134:135] op_sel_hi:[0,1]
	v_pk_mul_f32 v[136:137], v[164:165], v[136:137] op_sel_hi:[0,1]
	v_pk_mul_f32 v[164:165], v[108:109], v[132:133]
	v_pk_mul_f32 v[132:133], v[106:107], v[130:131]
	v_pk_mul_f32 v[136:137], v[116:117], v[136:137]
	v_pk_mul_f32 v[134:135], v[114:115], v[134:135]
	v_cvt_f32_i32_e32 v50, v50
	v_cvt_pk_bf16_f32 v130, v134, v135
	v_cvt_pk_bf16_f32 v131, v136, v137
	v_cvt_pk_bf16_f32 v132, v132, v133
	v_cvt_pk_bf16_f32 v133, v164, v165
	global_store_dwordx4 v[152:153], v[130:133], off
	v_cvt_f32_i32_e32 v57, v57
	v_cvt_f32_i32_e32 v56, v56
	v_or_b32_e32 v132, 16, v156
	v_ashrrev_i32_e32 v133, 31, v132
	v_lshlrev_b64 v[130:131], 12, v[132:133]
	v_lshl_add_u64 v[132:133], v[132:133], 2, s[40:41]
	s_nop 1
	v_lshl_add_u64 v[130:131], s[74:75], 0, v[130:131]
	v_lshl_add_u64 v[130:131], v[130:131], 0, v[158:159]
	v_cvt_f32_i32_e32 v55, v55
	v_cvt_f32_i32_e32 v54, v54
	v_cvt_f32_i32_e32 v45, v45
	v_cvt_f32_i32_e32 v44, v44
	v_cvt_f32_i32_e32 v43, v43
	v_cvt_f32_i32_e32 v42, v42
	v_cvt_f32_i32_e32 v49, v49
	v_cvt_f32_i32_e32 v48, v48
	v_cvt_f32_i32_e32 v47, v47
	v_cvt_f32_i32_e32 v46, v46
	v_cvt_f32_i32_e32 v37, v37
	v_cvt_f32_i32_e32 v36, v36
	v_cvt_f32_i32_e32 v35, v35
	v_cvt_f32_i32_e32 v34, v34
	v_cvt_f32_i32_e32 v41, v41
	v_cvt_f32_i32_e32 v40, v40
	v_cvt_f32_i32_e32 v39, v39
	v_cvt_f32_i32_e32 v38, v38
	v_cvt_f32_i32_e32 v29, v29
	v_cvt_f32_i32_e32 v28, v28
	v_cvt_f32_i32_e32 v27, v27
	v_cvt_f32_i32_e32 v26, v26
	v_cvt_f32_i32_e32 v33, v33
	v_cvt_f32_i32_e32 v32, v32
	v_cvt_f32_i32_e32 v31, v31
	v_cvt_f32_i32_e32 v30, v30
	v_cvt_f32_i32_e32 v21, v21
	v_cvt_f32_i32_e32 v20, v20
	v_cvt_f32_i32_e32 v19, v19
	v_cvt_f32_i32_e32 v18, v18
	v_cvt_f32_i32_e32 v25, v25
	v_cvt_f32_i32_e32 v24, v24
	v_cvt_f32_i32_e32 v23, v23
	v_cvt_f32_i32_e32 v22, v22
	v_cvt_f32_i32_e32 v13, v13
	v_cvt_f32_i32_e32 v12, v12
	v_cvt_f32_i32_e32 v11, v11
	v_cvt_f32_i32_e32 v10, v10
	v_cvt_f32_i32_e32 v17, v17
	v_cvt_f32_i32_e32 v16, v16
	v_cvt_f32_i32_e32 v15, v15
	v_cvt_f32_i32_e32 v14, v14
	v_cvt_f32_i32_e32 v5, v5
	v_cvt_f32_i32_e32 v4, v4
	v_cvt_f32_i32_e32 v3, v3
; __device__ __forceinline__ unsigned cvt_pk_bf16(float lo, float hi) { unsigned r; asm volatile("v_cvt_pk_bf16_f32 %0, %1, %2" : "=v"(r) : "v"(lo), "v"(hi)); return r; }
;     __device__ __forceinline__ void operator()(const f32x4 (&acc)[2][2][4][2], const Unit& u, int wr, int wc, int fr, int fq) const {
;     ...
;         for (int bj = 0; bj < 2; ++bj) {
;             const f32x4 s0 = *(const f32x4*)(sb + col0 + bj * HALF), s1 = *(const f32x4*)(sb + col0 + bj * HALF + 4);
; #pragma unroll
;             for (int ai = 0; ai < 2; ++ai)
; #pragma unroll
;                 for (int m = 0; m < 4; ++m) { const int row = row0 + ai * HALF + m * 16; bf16_t* rowp = O + (size_t)row * ldc + col0 + bj * HALF;
;                     f32x4 v0, v1;
;                     if constexpr (I8) { const float ra = sa[row]; const i32x4 i0 = __builtin_bit_cast(i32x4, acc[ai][bj][m][0]), i1 = __builtin_bit_cast(i32x4, acc[ai][bj][m][1]);
;                         v0 = __builtin_convertvector(i0, f32x4) * ra * s0; v1 = __builtin_convertvector(i1, f32x4) * ra * s1; }
;                     else { v0 = acc[ai][bj][m][0] * s0; v1 = acc[ai][bj][m][1] * s1; }
;                     u32x4 w; w.x = cvt_pk_bf16(v0[0], v0[1]); w.y = cvt_pk_bf16(v0[2], v0[3]); w.z = cvt_pk_bf16(v1[0], v1[1]); w.w = cvt_pk_bf16(v1[2], v1[3]);
;                     *(u32x4*)rowp = w; }
	v_cvt_f32_i32_e32 v2, v2
	v_cvt_f32_i32_e32 v9, v9
	v_cvt_f32_i32_e32 v8, v8
	v_cvt_f32_i32_e32 v7, v7
	v_cvt_f32_i32_e32 v6, v6
	v_pk_mul_f32 v[122:123], v[180:181], v[122:123] op_sel_hi:[0,1]
	v_pk_mul_f32 v[124:125], v[180:181], v[124:125] op_sel_hi:[0,1]
	v_pk_mul_f32 v[126:127], v[180:181], v[126:127] op_sel_hi:[0,1]
	v_pk_mul_f32 v[128:129], v[180:181], v[128:129] op_sel_hi:[0,1]
	v_pk_mul_f32 v[134:135], v[108:109], v[124:125]
	v_pk_mul_f32 v[124:125], v[106:107], v[122:123]
	v_pk_mul_f32 v[128:129], v[116:117], v[128:129]
	v_pk_mul_f32 v[126:127], v[114:115], v[126:127]
	s_nop 0
	v_cvt_pk_bf16_f32 v122, v126, v127
	v_cvt_pk_bf16_f32 v123, v128, v129
	v_cvt_pk_bf16_f32 v124, v124, v125
	v_cvt_pk_bf16_f32 v125, v134, v135
	global_store_dwordx4 v[130:131], v[122:125], off
	s_nop 1
	v_or_b32_e32 v124, 32, v156
	v_ashrrev_i32_e32 v125, 31, v124
	v_lshlrev_b64 v[122:123], 12, v[124:125]
	v_lshl_add_u64 v[124:125], v[124:125], 2, s[40:41]
	s_nop 1
	v_lshl_add_u64 v[122:123], s[74:75], 0, v[122:123]
	v_lshl_add_u64 v[122:123], v[122:123], 0, v[158:159]
	v_pk_mul_f32 v[110:111], v[182:183], v[110:111] op_sel_hi:[0,1]
	v_pk_mul_f32 v[112:113], v[182:183], v[112:113] op_sel_hi:[0,1]
	v_pk_mul_f32 v[118:119], v[182:183], v[118:119] op_sel_hi:[0,1]
	v_pk_mul_f32 v[120:121], v[182:183], v[120:121] op_sel_hi:[0,1]
	v_pk_mul_f32 v[126:127], v[108:109], v[112:113]
	v_pk_mul_f32 v[112:113], v[106:107], v[110:111]
	v_pk_mul_f32 v[120:121], v[116:117], v[120:121]
	v_pk_mul_f32 v[118:119], v[114:115], v[118:119]
	s_nop 0
	v_cvt_pk_bf16_f32 v110, v118, v119
	v_cvt_pk_bf16_f32 v111, v120, v121
	v_cvt_pk_bf16_f32 v112, v112, v113
	v_cvt_pk_bf16_f32 v113, v126, v127
	global_store_dwordx4 v[122:123], v[110:113], off
	s_nop 1
	v_or_b32_e32 v112, 48, v156
	v_ashrrev_i32_e32 v113, 31, v112
	v_lshlrev_b64 v[110:111], 12, v[112:113]
	v_lshl_add_u64 v[112:113], v[112:113], 2, s[40:41]
	s_nop 1
	v_lshl_add_u64 v[110:111], s[74:75], 0, v[110:111]
	v_lshl_add_u64 v[110:111], v[110:111], 0, v[158:159]
	v_pk_mul_f32 v[98:99], v[184:185], v[98:99] op_sel_hi:[0,1]
	v_pk_mul_f32 v[100:101], v[184:185], v[100:101] op_sel_hi:[0,1]
	v_pk_mul_f32 v[102:103], v[184:185], v[102:103] op_sel_hi:[0,1]
	v_pk_mul_f32 v[104:105], v[184:185], v[104:105] op_sel_hi:[0,1]
	v_pk_mul_f32 v[118:119], v[108:109], v[100:101]
	v_pk_mul_f32 v[100:101], v[106:107], v[98:99]
	v_pk_mul_f32 v[104:105], v[116:117], v[104:105]
	v_pk_mul_f32 v[102:103], v[114:115], v[102:103]
	s_nop 0
	v_cvt_pk_bf16_f32 v98, v102, v103
	v_cvt_pk_bf16_f32 v99, v104, v105
	v_cvt_pk_bf16_f32 v100, v100, v101
	v_cvt_pk_bf16_f32 v101, v118, v119
	global_store_dwordx4 v[110:111], v[98:101], off
	s_nop 1
	v_pk_mul_f32 v[94:95], v[186:187], v[94:95] op_sel_hi:[0,1]
	v_lshl_add_u64 v[98:99], v[152:153], 0, s[6:7]
	v_pk_mul_f32 v[94:95], v[114:115], v[94:95]
	v_pk_mul_f32 v[90:91], v[186:187], v[90:91] op_sel_hi:[0,1]
	v_pk_mul_f32 v[92:93], v[186:187], v[92:93] op_sel_hi:[0,1]
	s_mov_b32 s6, 0x80000
	v_pk_mul_f32 v[96:97], v[186:187], v[96:97] op_sel_hi:[0,1]
	v_pk_mul_f32 v[100:101], v[108:109], v[92:93]
	v_pk_mul_f32 v[92:93], v[106:107], v[90:91]
	v_cvt_pk_bf16_f32 v90, v94, v95
	v_add_co_u32_e32 v94, vcc, s6, v152
	v_pk_mul_f32 v[96:97], v[116:117], v[96:97]
	s_nop 0
	v_addc_co_u32_e32 v95, vcc, 0, v153, vcc
	v_cvt_pk_bf16_f32 v91, v96, v97
	v_cvt_pk_bf16_f32 v92, v92, v93
	v_cvt_pk_bf16_f32 v93, v100, v101
	global_store_dwordx4 v[94:95], v[90:93], off
	s_nop 1
	s_mov_b64 s[6:7], 0x90000
	v_lshl_add_u64 v[90:91], v[152:153], 0, s[6:7]
	s_mov_b32 s6, 0x90000
	v_pk_mul_f32 v[86:87], v[188:189], v[86:87] op_sel_hi:[0,1]
	v_pk_mul_f32 v[86:87], v[114:115], v[86:87]
	v_pk_mul_f32 v[82:83], v[188:189], v[82:83] op_sel_hi:[0,1]
	v_pk_mul_f32 v[84:85], v[188:189], v[84:85] op_sel_hi:[0,1]
	v_pk_mul_f32 v[88:89], v[188:189], v[88:89] op_sel_hi:[0,1]
	v_pk_mul_f32 v[92:93], v[108:109], v[84:85]
	v_pk_mul_f32 v[84:85], v[106:107], v[82:83]
	v_cvt_pk_bf16_f32 v82, v86, v87
	v_add_co_u32_e32 v86, vcc, s6, v152
	v_pk_mul_f32 v[88:89], v[116:117], v[88:89]
	s_nop 0
	v_addc_co_u32_e32 v87, vcc, 0, v153, vcc
	v_cvt_pk_bf16_f32 v83, v88, v89
	v_cvt_pk_bf16_f32 v84, v84, v85
	v_cvt_pk_bf16_f32 v85, v92, v93
	global_store_dwordx4 v[86:87], v[82:85], off
	s_nop 1
	s_mov_b64 s[6:7], 0xa0000
	v_lshl_add_u64 v[82:83], v[152:153], 0, s[6:7]
	s_mov_b32 s6, 0xa0000
	v_pk_mul_f32 v[78:79], v[190:191], v[78:79] op_sel_hi:[0,1]
	v_pk_mul_f32 v[78:79], v[114:115], v[78:79]
	v_pk_mul_f32 v[74:75], v[190:191], v[74:75] op_sel_hi:[0,1]
	v_pk_mul_f32 v[76:77], v[190:191], v[76:77] op_sel_hi:[0,1]
	v_pk_mul_f32 v[80:81], v[190:191], v[80:81] op_sel_hi:[0,1]
	v_pk_mul_f32 v[84:85], v[108:109], v[76:77]
	v_pk_mul_f32 v[76:77], v[106:107], v[74:75]
	v_cvt_pk_bf16_f32 v74, v78, v79
	v_add_co_u32_e32 v78, vcc, s6, v152
	v_pk_mul_f32 v[80:81], v[116:117], v[80:81]
	s_nop 0
	v_addc_co_u32_e32 v79, vcc, 0, v153, vcc
	v_cvt_pk_bf16_f32 v75, v80, v81
	v_cvt_pk_bf16_f32 v76, v76, v77
	v_cvt_pk_bf16_f32 v77, v84, v85
	global_store_dwordx4 v[78:79], v[74:77], off
	s_nop 1
	s_mov_b64 s[6:7], 0xb0000
	v_lshl_add_u64 v[74:75], v[152:153], 0, s[6:7]
	s_mov_b32 s6, 0xb0000
	v_pk_mul_f32 v[70:71], v[192:193], v[70:71] op_sel_hi:[0,1]
	v_pk_mul_f32 v[70:71], v[114:115], v[70:71]
	v_pk_mul_f32 v[66:67], v[192:193], v[66:67] op_sel_hi:[0,1]
	v_pk_mul_f32 v[68:69], v[192:193], v[68:69] op_sel_hi:[0,1]
	v_pk_mul_f32 v[72:73], v[192:193], v[72:73] op_sel_hi:[0,1]
	v_pk_mul_f32 v[76:77], v[108:109], v[68:69]
	v_pk_mul_f32 v[68:69], v[106:107], v[66:67]
; __device__ __forceinline__ unsigned cvt_pk_bf16(float lo, float hi) { unsigned r; asm volatile("v_cvt_pk_bf16_f32 %0, %1, %2" : "=v"(r) : "v"(lo), "v"(hi)); return r; }
; #define PG8_BAR __builtin_amdgcn_s_barrier()
;     __device__ __forceinline__ void operator()(const f32x4 (&acc)[2][2][4][2], const Unit& u, int wr, int wc, int fr, int fq) const {
;     ...
;         for (int bj = 0; bj < 2; ++bj) {
;             const f32x4 s0 = *(const f32x4*)(sb + col0 + bj * HALF), s1 = *(const f32x4*)(sb + col0 + bj * HALF + 4);
; #pragma unroll
;             for (int ai = 0; ai < 2; ++ai)
; #pragma unroll
;                 for (int m = 0; m < 4; ++m) { const int row = row0 + ai * HALF + m * 16; bf16_t* rowp = O + (size_t)row * ldc + col0 + bj * HALF;
;                     f32x4 v0, v1;
;                     if constexpr (I8) { const float ra = sa[row]; const i32x4 i0 = __builtin_bit_cast(i32x4, acc[ai][bj][m][0]), i1 = __builtin_bit_cast(i32x4, acc[ai][bj][m][1]);
;                         v0 = __builtin_convertvector(i0, f32x4) * ra * s0; v1 = __builtin_convertvector(i1, f32x4) * ra * s1; }
;                     else { v0 = acc[ai][bj][m][0] * s0; v1 = acc[ai][bj][m][1] * s1; }
;                     u32x4 w; w.x = cvt_pk_bf16(v0[0], v0[1]); w.y = cvt_pk_bf16(v0[2], v0[3]); w.z = cvt_pk_bf16(v1[0], v1[1]); w.w = cvt_pk_bf16(v1[2], v1[3]);
;                     *(u32x4*)rowp = w; }
;     ...
;         if (!has_next) break;
; #pragma unroll
;         for (int a = 0; a < 2; ++a)
; #pragma unroll
;             for (int b = 0; b < 2; ++b)
; #pragma unroll
;                 for (int m = 0; m < 4; ++m)
; #pragma unroll
;                     for (int n = 0; n < 2; ++n) acc[a][b][m][n] = (f32x4){0.f, 0.f, 0.f, 0.f};
;         cur = nxt; cA = nA; cB = nB; ++ui;
;         if constexpr (ALIGN_EPI) { if (wr == 1) PG8_BAR; }
	v_cvt_pk_bf16_f32 v66, v70, v71
	v_add_co_u32_e32 v70, vcc, s6, v152
	v_pk_mul_f32 v[72:73], v[116:117], v[72:73]
	s_nop 0
	v_addc_co_u32_e32 v71, vcc, 0, v153, vcc
	v_cvt_pk_bf16_f32 v67, v72, v73
	v_cvt_pk_bf16_f32 v68, v68, v69
	v_cvt_pk_bf16_f32 v69, v76, v77
	global_store_dwordx4 v[70:71], v[66:69], off
	s_nop 0
	s_nop 1
	s_mov_b64 s[6:7], -1
	s_andn2_b64 vcc, exec, s[38:39]
	v_pk_mul_f32 v[58:59], v[178:179], v[58:59] op_sel_hi:[0,1]
	v_pk_mul_f32 v[60:61], v[178:179], v[60:61] op_sel_hi:[0,1]
	v_pk_mul_f32 v[62:63], v[178:179], v[62:63] op_sel_hi:[0,1]
	v_pk_mul_f32 v[64:65], v[178:179], v[64:65] op_sel_hi:[0,1]
	v_pk_mul_f32 v[76:77], v[196:197], v[60:61]
	v_pk_mul_f32 v[60:61], v[194:195], v[58:59]
	v_pk_mul_f32 v[64:65], v[200:201], v[64:65]
	v_pk_mul_f32 v[62:63], v[198:199], v[62:63]
	s_nop 0
	v_cvt_pk_bf16_f32 v58, v62, v63
	v_cvt_pk_bf16_f32 v59, v64, v65
	v_cvt_pk_bf16_f32 v60, v60, v61
	v_cvt_pk_bf16_f32 v61, v76, v77
	global_store_dwordx4 v[152:153], v[58:61], off offset:256
	s_nop 1
	v_pk_mul_f32 v[50:51], v[180:181], v[50:51] op_sel_hi:[0,1]
	v_pk_mul_f32 v[52:53], v[180:181], v[52:53] op_sel_hi:[0,1]
	v_pk_mul_f32 v[54:55], v[180:181], v[54:55] op_sel_hi:[0,1]
	v_pk_mul_f32 v[56:57], v[180:181], v[56:57] op_sel_hi:[0,1]
	v_pk_mul_f32 v[58:59], v[196:197], v[52:53]
	v_pk_mul_f32 v[52:53], v[194:195], v[50:51]
	v_pk_mul_f32 v[56:57], v[200:201], v[56:57]
	v_pk_mul_f32 v[54:55], v[198:199], v[54:55]
	s_nop 0
	v_cvt_pk_bf16_f32 v50, v54, v55
	v_cvt_pk_bf16_f32 v51, v56, v57
	v_cvt_pk_bf16_f32 v52, v52, v53
	v_cvt_pk_bf16_f32 v53, v58, v59
	global_store_dwordx4 v[130:131], v[50:53], off offset:256
	s_nop 1
	v_pk_mul_f32 v[42:43], v[182:183], v[42:43] op_sel_hi:[0,1]
	v_pk_mul_f32 v[44:45], v[182:183], v[44:45] op_sel_hi:[0,1]
	v_pk_mul_f32 v[46:47], v[182:183], v[46:47] op_sel_hi:[0,1]
	v_pk_mul_f32 v[48:49], v[182:183], v[48:49] op_sel_hi:[0,1]
	v_pk_mul_f32 v[50:51], v[196:197], v[44:45]
	v_pk_mul_f32 v[44:45], v[194:195], v[42:43]
	v_pk_mul_f32 v[48:49], v[200:201], v[48:49]
	v_pk_mul_f32 v[46:47], v[198:199], v[46:47]
	s_nop 0
	v_cvt_pk_bf16_f32 v42, v46, v47
	v_cvt_pk_bf16_f32 v43, v48, v49
	v_cvt_pk_bf16_f32 v44, v44, v45
	v_cvt_pk_bf16_f32 v45, v50, v51
	global_store_dwordx4 v[122:123], v[42:45], off offset:256
	s_nop 1
	v_pk_mul_f32 v[34:35], v[184:185], v[34:35] op_sel_hi:[0,1]
	v_pk_mul_f32 v[36:37], v[184:185], v[36:37] op_sel_hi:[0,1]
	v_pk_mul_f32 v[38:39], v[184:185], v[38:39] op_sel_hi:[0,1]
	v_pk_mul_f32 v[40:41], v[184:185], v[40:41] op_sel_hi:[0,1]
	v_pk_mul_f32 v[42:43], v[196:197], v[36:37]
	v_pk_mul_f32 v[36:37], v[194:195], v[34:35]
	v_pk_mul_f32 v[40:41], v[200:201], v[40:41]
	v_pk_mul_f32 v[38:39], v[198:199], v[38:39]
	s_nop 0
	v_cvt_pk_bf16_f32 v34, v38, v39
	v_cvt_pk_bf16_f32 v35, v40, v41
	v_cvt_pk_bf16_f32 v36, v36, v37
	v_cvt_pk_bf16_f32 v37, v42, v43
	global_store_dwordx4 v[110:111], v[34:37], off offset:256
	s_nop 1
	v_pk_mul_f32 v[26:27], v[186:187], v[26:27] op_sel_hi:[0,1]
	v_pk_mul_f32 v[28:29], v[186:187], v[28:29] op_sel_hi:[0,1]
	v_pk_mul_f32 v[30:31], v[186:187], v[30:31] op_sel_hi:[0,1]
	v_pk_mul_f32 v[32:33], v[186:187], v[32:33] op_sel_hi:[0,1]
	v_pk_mul_f32 v[34:35], v[196:197], v[28:29]
	v_pk_mul_f32 v[28:29], v[194:195], v[26:27]
	v_pk_mul_f32 v[32:33], v[200:201], v[32:33]
	v_pk_mul_f32 v[30:31], v[198:199], v[30:31]
	s_nop 0
	v_cvt_pk_bf16_f32 v26, v30, v31
	v_cvt_pk_bf16_f32 v27, v32, v33
	v_cvt_pk_bf16_f32 v28, v28, v29
	v_cvt_pk_bf16_f32 v29, v34, v35
	global_store_dwordx4 v[98:99], v[26:29], off offset:256
	s_nop 1
	v_pk_mul_f32 v[18:19], v[188:189], v[18:19] op_sel_hi:[0,1]
	v_pk_mul_f32 v[20:21], v[188:189], v[20:21] op_sel_hi:[0,1]
	v_pk_mul_f32 v[22:23], v[188:189], v[22:23] op_sel_hi:[0,1]
	v_pk_mul_f32 v[24:25], v[188:189], v[24:25] op_sel_hi:[0,1]
	v_pk_mul_f32 v[26:27], v[196:197], v[20:21]
	v_pk_mul_f32 v[20:21], v[194:195], v[18:19]
	v_pk_mul_f32 v[24:25], v[200:201], v[24:25]
	v_pk_mul_f32 v[22:23], v[198:199], v[22:23]
	s_nop 0
	v_cvt_pk_bf16_f32 v18, v22, v23
	v_cvt_pk_bf16_f32 v19, v24, v25
	v_cvt_pk_bf16_f32 v20, v20, v21
	v_cvt_pk_bf16_f32 v21, v26, v27
	global_store_dwordx4 v[90:91], v[18:21], off offset:256
	s_nop 1
	v_pk_mul_f32 v[10:11], v[190:191], v[10:11] op_sel_hi:[0,1]
	v_pk_mul_f32 v[12:13], v[190:191], v[12:13] op_sel_hi:[0,1]
	v_pk_mul_f32 v[14:15], v[190:191], v[14:15] op_sel_hi:[0,1]
	v_pk_mul_f32 v[16:17], v[190:191], v[16:17] op_sel_hi:[0,1]
	v_pk_mul_f32 v[18:19], v[196:197], v[12:13]
	v_pk_mul_f32 v[12:13], v[194:195], v[10:11]
	v_pk_mul_f32 v[16:17], v[200:201], v[16:17]
	v_pk_mul_f32 v[14:15], v[198:199], v[14:15]
	s_nop 0
	v_cvt_pk_bf16_f32 v10, v14, v15
	v_cvt_pk_bf16_f32 v11, v16, v17
	v_cvt_pk_bf16_f32 v12, v12, v13
	v_cvt_pk_bf16_f32 v13, v18, v19
	global_store_dwordx4 v[82:83], v[10:13], off offset:256
	s_nop 1
	v_pk_mul_f32 v[2:3], v[192:193], v[2:3] op_sel_hi:[0,1]
	v_pk_mul_f32 v[4:5], v[192:193], v[4:5] op_sel_hi:[0,1]
	v_pk_mul_f32 v[6:7], v[192:193], v[6:7] op_sel_hi:[0,1]
	v_pk_mul_f32 v[8:9], v[192:193], v[8:9] op_sel_hi:[0,1]
	v_pk_mul_f32 v[10:11], v[196:197], v[4:5]
	v_pk_mul_f32 v[4:5], v[194:195], v[2:3]
	v_pk_mul_f32 v[8:9], v[200:201], v[8:9]
	v_pk_mul_f32 v[6:7], v[198:199], v[6:7]
	s_nop 0
	v_cvt_pk_bf16_f32 v2, v6, v7
	v_cvt_pk_bf16_f32 v3, v8, v9
	v_cvt_pk_bf16_f32 v4, v4, v5
	v_cvt_pk_bf16_f32 v5, v10, v11
	global_store_dwordx4 v[74:75], v[2:5], off offset:256
	s_cbranch_vccnz .LBB0_618
	s_andn2_b64 vcc, exec, s[0:1]
	s_cbranch_vccnz .LBB0_617
	s_barrier
	s_branch .LBB0_617

; __device__ __forceinline__ unsigned xb_ld(unsigned* p)              { return __hip_atomic_load(p, __ATOMIC_RELAXED, __HIP_MEMORY_SCOPE_AGENT); }
; __device__ __forceinline__ unsigned xb_add(unsigned* p, unsigned v) { return __hip_atomic_fetch_add(p, v, __ATOMIC_RELAXED, __HIP_MEMORY_SCOPE_AGENT); }
; #define XB_SPIN(cond, bar) do { unsigned _sp = 0; while (cond) { __builtin_amdgcn_s_sleep(1); \
;     if ((++_sp & 255u) == 0u) { if (xb_ld(&(bar)[XB_TMO])) break; if (_sp > XB_SPIN_CAP) { atomicAdd(&(bar)[XB_TMO], 1u); break; } } } } while (0)
; __device__ __forceinline__ void xcd_barrier(const XcdBarrier& b) {
;     ...
;         const unsigned old = xb_add(&bar[XB_XSUB(b.x)], 1u);
;         const unsigned gen = old / nloc;
;         if (old + 1u == (gen + 1u) * nloc) {
;             __builtin_amdgcn_fence(__ATOMIC_RELEASE, "agent");
;             asm volatile("s_waitcnt vmcnt(0)" ::: "memory");
;             const unsigned og = xb_add(&bar[XB_TOP], 1u);
;             const unsigned tg = og / nx;
;             if (og + 1u == (tg + 1u) * nx) xb_add(&bar[XB_TOPGEN], 1u);
;             else XB_SPIN(xb_ld(&bar[XB_TOPGEN]) == tg, bar);
;             __builtin_amdgcn_fence(__ATOMIC_ACQUIRE, "agent");
;             xb_add(&bar[XB_XGEN(b.x)], 1u);
;             asm volatile("s_waitcnt vmcnt(0)" ::: "memory");
;         } else {
;             XB_SPIN(xb_ld(&bar[XB_XGEN(b.x)]) == gen, bar);
.LBB0_789:
	s_or_b64 exec, exec, s[2:3]
	buffer_inv sc1
	v_cvt_f32_u32_e32 v5, v3
	s_waitcnt vmcnt(1)
	v_readfirstlane_b32 s2, v4
	v_sub_u32_e32 v4, 0, v3
	v_rcp_iflag_f32_e32 v5, v5
	v_add_u32_e32 v6, s2, v1
	v_mul_f32_e32 v5, 0x4f7ffffe, v5
	v_cvt_u32_f32_e32 v5, v5
	v_mul_lo_u32 v1, v4, v5
	v_mul_hi_u32 v1, v5, v1
	v_add_u32_e32 v1, v5, v1
	v_mul_hi_u32 v1, v6, v1
	v_mul_lo_u32 v4, v1, v3
	v_sub_u32_e32 v4, v6, v4
	v_add_u32_e32 v5, 1, v1
	v_cmp_ge_u32_e32 vcc, v4, v3
	s_nop 1
	v_cndmask_b32_e32 v1, v1, v5, vcc
	v_sub_u32_e32 v5, v4, v3
	v_cndmask_b32_e32 v4, v4, v5, vcc
	v_add_u32_e32 v5, 1, v1
	v_cmp_ge_u32_e32 vcc, v4, v3
	v_add_u32_e32 v4, 1, v6
	s_nop 0
	v_cndmask_b32_e32 v1, v1, v5, vcc
	v_mul_lo_u32 v5, v3, v1
	v_add_u32_e32 v3, v5, v3
	v_cmp_ne_u32_e32 vcc, v4, v3
	s_and_saveexec_b64 s[2:3], vcc
	s_xor_b64 s[2:3], exec, s[2:3]
	s_cbranch_execz .LBB0_803
	v_readlane_b32 s4, v242, 22
	s_waitcnt lgkmcnt(0)
	v_mov_b32_e32 v2, 0
	v_readlane_b32 s5, v242, 23
	s_nop 4
	global_load_dword v3, v2, s[4:5] sc1
	s_waitcnt vmcnt(0)
	v_cmp_eq_u32_e32 vcc, v3, v1
	s_and_saveexec_b64 s[4:5], vcc
	s_cbranch_execz .LBB0_802
	s_mov_b32 s8, 1
	s_mov_b64 s[6:7], 0
	s_branch .LBB0_793

; __device__ __forceinline__ unsigned xb_ld(unsigned* p)              { return __hip_atomic_load(p, __ATOMIC_RELAXED, __HIP_MEMORY_SCOPE_AGENT); }
; #define XB_SPIN(cond, bar) do { unsigned _sp = 0; while (cond) { __builtin_amdgcn_s_sleep(1); \
;     if ((++_sp & 255u) == 0u) { if (xb_ld(&(bar)[XB_TMO])) break; if (_sp > XB_SPIN_CAP) { atomicAdd(&(bar)[XB_TMO], 1u); break; } } } } while (0)
; __device__ __forceinline__ void xcd_barrier(const XcdBarrier& b) {
;     ...
;             XB_SPIN(xb_ld(&bar[XB_XGEN(b.x)]) == gen, bar);
;             __builtin_amdgcn_fence(__ATOMIC_ACQUIRE, "agent");
;             asm volatile("s_waitcnt vmcnt(0)" ::: "memory");
.LBB0_802:
	s_or_b64 exec, exec, s[4:5]
	s_waitcnt vmcnt(0)
	s_waitcnt vmcnt(0)

; __device__ __forceinline__ unsigned xb_ld(unsigned* p)              { return __hip_atomic_load(p, __ATOMIC_RELAXED, __HIP_MEMORY_SCOPE_AGENT); }
; __device__ __forceinline__ unsigned xb_add(unsigned* p, unsigned v) { return __hip_atomic_fetch_add(p, v, __ATOMIC_RELAXED, __HIP_MEMORY_SCOPE_AGENT); }
; #define XB_SPIN(cond, bar) do { unsigned _sp = 0; while (cond) { __builtin_amdgcn_s_sleep(1); \
;     if ((++_sp & 255u) == 0u) { if (xb_ld(&(bar)[XB_TMO])) break; if (_sp > XB_SPIN_CAP) { atomicAdd(&(bar)[XB_TMO], 1u); break; } } } } while (0)
; __device__ __forceinline__ void xcd_barrier(const XcdBarrier& b) {
;     ...
;             else XB_SPIN(xb_ld(&bar[XB_TOPGEN]) == tg, bar);
;             __builtin_amdgcn_fence(__ATOMIC_ACQUIRE, "agent");
;             xb_add(&bar[XB_XGEN(b.x)], 1u);
;             asm volatile("s_waitcnt vmcnt(0)" ::: "memory");
.LBB0_820:
	s_or_b64 exec, exec, s[2:3]
	s_mov_b64 s[2:3], exec
	v_mbcnt_lo_u32_b32 v1, s2, 0
	v_mbcnt_hi_u32_b32 v1, s3, v1
	v_cmp_eq_u32_e32 vcc, 0, v1
	s_waitcnt vmcnt(0)
	s_and_saveexec_b64 s[4:5], vcc
	s_cbranch_execz .LBB0_822
	s_bcnt1_i32_b64 s2, s[2:3]
	v_mov_b32_e32 v2, s2
	v_readlane_b32 s2, v242, 22
	v_mov_b32_e32 v1, 0
	v_readlane_b32 s3, v242, 23
	s_nop 4
	global_atomic_add v1, v2, s[2:3]

; __device__ __forceinline__ unsigned xb_ld(unsigned* p)              { return __hip_atomic_load(p, __ATOMIC_RELAXED, __HIP_MEMORY_SCOPE_AGENT); }
; __device__ __forceinline__ unsigned xb_add(unsigned* p, unsigned v) { return __hip_atomic_fetch_add(p, v, __ATOMIC_RELAXED, __HIP_MEMORY_SCOPE_AGENT); }
; #define XB_SPIN(cond, bar) do { unsigned _sp = 0; while (cond) { __builtin_amdgcn_s_sleep(1); \
;     if ((++_sp & 255u) == 0u) { if (xb_ld(&(bar)[XB_TMO])) break; if (_sp > XB_SPIN_CAP) { atomicAdd(&(bar)[XB_TMO], 1u); break; } } } } while (0)
; __device__ __forceinline__ void xcd_barrier(const XcdBarrier& b) {
;     ...
;         const unsigned old = xb_add(&bar[XB_XSUB(b.x)], 1u);
;         const unsigned gen = old / nloc;
;         if (old + 1u == (gen + 1u) * nloc) {
;             __builtin_amdgcn_fence(__ATOMIC_RELEASE, "agent");
;             asm volatile("s_waitcnt vmcnt(0)" ::: "memory");
;             const unsigned og = xb_add(&bar[XB_TOP], 1u);
;             const unsigned tg = og / nx;
;             if (og + 1u == (tg + 1u) * nx) xb_add(&bar[XB_TOPGEN], 1u);
;             else XB_SPIN(xb_ld(&bar[XB_TOPGEN]) == tg, bar);
;             __builtin_amdgcn_fence(__ATOMIC_ACQUIRE, "agent");
;             xb_add(&bar[XB_XGEN(b.x)], 1u);
;             asm volatile("s_waitcnt vmcnt(0)" ::: "memory");
;         } else {
;             XB_SPIN(xb_ld(&bar[XB_XGEN(b.x)]) == gen, bar);
.LBB0_848:
	s_or_b64 exec, exec, s[2:3]
	buffer_inv sc1
	v_cvt_f32_u32_e32 v5, v3
	s_waitcnt vmcnt(1)
	v_readfirstlane_b32 s2, v4
	v_sub_u32_e32 v4, 0, v3
	v_rcp_iflag_f32_e32 v5, v5
	v_add_u32_e32 v6, s2, v2
	v_mul_f32_e32 v5, 0x4f7ffffe, v5
	v_cvt_u32_f32_e32 v5, v5
	v_mul_lo_u32 v2, v4, v5
	v_mul_hi_u32 v2, v5, v2
	v_add_u32_e32 v2, v5, v2
	v_mul_hi_u32 v2, v6, v2
	v_mul_lo_u32 v4, v2, v3
	v_sub_u32_e32 v4, v6, v4
	v_add_u32_e32 v5, 1, v2
	v_cmp_ge_u32_e32 vcc, v4, v3
	s_nop 1
	v_cndmask_b32_e32 v2, v2, v5, vcc
	v_sub_u32_e32 v5, v4, v3
	v_cndmask_b32_e32 v4, v4, v5, vcc
	v_add_u32_e32 v5, 1, v2
	v_cmp_ge_u32_e32 vcc, v4, v3
	v_add_u32_e32 v4, 1, v6
	s_nop 0
	v_cndmask_b32_e32 v2, v2, v5, vcc
	v_mul_lo_u32 v5, v3, v2
	v_add_u32_e32 v3, v5, v3
	v_cmp_ne_u32_e32 vcc, v4, v3
	s_and_saveexec_b64 s[2:3], vcc
	s_xor_b64 s[2:3], exec, s[2:3]
	s_cbranch_execz .LBB0_862
	v_readlane_b32 s4, v242, 22
	s_waitcnt lgkmcnt(0)
	v_mov_b32_e32 v1, 0
	v_readlane_b32 s5, v242, 23
	s_nop 4
	global_load_dword v3, v1, s[4:5] sc1
	s_waitcnt vmcnt(0)
	v_cmp_eq_u32_e32 vcc, v3, v2
	s_and_saveexec_b64 s[4:5], vcc
	s_cbranch_execz .LBB0_861
	s_mov_b32 s8, 1
	s_mov_b64 s[6:7], 0
	s_branch .LBB0_852

; __device__ __forceinline__ unsigned xb_ld(unsigned* p)              { return __hip_atomic_load(p, __ATOMIC_RELAXED, __HIP_MEMORY_SCOPE_AGENT); }
; __device__ __forceinline__ unsigned xb_add(unsigned* p, unsigned v) { return __hip_atomic_fetch_add(p, v, __ATOMIC_RELAXED, __HIP_MEMORY_SCOPE_AGENT); }
; #define XB_SPIN(cond, bar) do { unsigned _sp = 0; while (cond) { __builtin_amdgcn_s_sleep(1); \
;     if ((++_sp & 255u) == 0u) { if (xb_ld(&(bar)[XB_TMO])) break; if (_sp > XB_SPIN_CAP) { atomicAdd(&(bar)[XB_TMO], 1u); break; } } } } while (0)
; __device__ __forceinline__ void xcd_barrier(const XcdBarrier& b) {
;     ...
;         const unsigned old = xb_add(&bar[XB_XSUB(b.x)], 1u);
;         const unsigned gen = old / nloc;
;         if (old + 1u == (gen + 1u) * nloc) {
;             __builtin_amdgcn_fence(__ATOMIC_RELEASE, "agent");
;             asm volatile("s_waitcnt vmcnt(0)" ::: "memory");
;             const unsigned og = xb_add(&bar[XB_TOP], 1u);
;             const unsigned tg = og / nx;
;             if (og + 1u == (tg + 1u) * nx) xb_add(&bar[XB_TOPGEN], 1u);
;             else XB_SPIN(xb_ld(&bar[XB_TOPGEN]) == tg, bar);
;             __builtin_amdgcn_fence(__ATOMIC_ACQUIRE, "agent");
;             xb_add(&bar[XB_XGEN(b.x)], 1u);
;             asm volatile("s_waitcnt vmcnt(0)" ::: "memory");
;         } else {
;             XB_SPIN(xb_ld(&bar[XB_XGEN(b.x)]) == gen, bar);
.LBB0_968:
	s_or_b64 exec, exec, s[2:3]
	buffer_inv sc1
	v_cvt_f32_u32_e32 v5, v3
	s_waitcnt vmcnt(1)
	v_readfirstlane_b32 s2, v4
	v_sub_u32_e32 v4, 0, v3
	v_rcp_iflag_f32_e32 v5, v5
	v_add_u32_e32 v6, s2, v2
	v_mul_f32_e32 v5, 0x4f7ffffe, v5
	v_cvt_u32_f32_e32 v5, v5
	v_mul_lo_u32 v2, v4, v5
	v_mul_hi_u32 v2, v5, v2
	v_add_u32_e32 v2, v5, v2
	v_mul_hi_u32 v2, v6, v2
	v_mul_lo_u32 v4, v2, v3
	v_sub_u32_e32 v4, v6, v4
	v_add_u32_e32 v5, 1, v2
	v_cmp_ge_u32_e32 vcc, v4, v3
	s_nop 1
	v_cndmask_b32_e32 v2, v2, v5, vcc
	v_sub_u32_e32 v5, v4, v3
	v_cndmask_b32_e32 v4, v4, v5, vcc
	v_add_u32_e32 v5, 1, v2
	v_cmp_ge_u32_e32 vcc, v4, v3
	v_add_u32_e32 v4, 1, v6
	s_nop 0
	v_cndmask_b32_e32 v2, v2, v5, vcc
	v_mul_lo_u32 v5, v3, v2
	v_add_u32_e32 v3, v5, v3
	v_cmp_ne_u32_e32 vcc, v4, v3
	s_and_saveexec_b64 s[2:3], vcc
	s_xor_b64 s[2:3], exec, s[2:3]
	s_cbranch_execz .LBB0_982
	v_readlane_b32 s4, v242, 22
	s_waitcnt lgkmcnt(0)
	v_mov_b32_e32 v1, 0
	v_readlane_b32 s5, v242, 23
	s_nop 4
	global_load_dword v3, v1, s[4:5] sc1
	s_waitcnt vmcnt(0)
	v_cmp_eq_u32_e32 vcc, v3, v2
	s_and_saveexec_b64 s[4:5], vcc
	s_cbranch_execz .LBB0_981
	s_mov_b32 s16, 1
	s_mov_b64 s[6:7], 0
	s_branch .LBB0_972
